# P11 sweep U rewritten by hand: 16 B per lane / half a wave per 512-B table row (one dwordx4 load per two rows), 32-lane row reduction; fixes a DPP wait-state gap
# speedup vs baseline: 1.0509x; 1.0118x over previous
; #define LAS __attribute__((address_space(3)))
; #define PE_VMW "vmcnt(" PE_STR(PE_VMY) ")"
; #define PE_ISSUE_U(S, rec_) PE_ISSUE4(S, rec_, UB8)
; #define PE_WAIT4U(S, cntstr) asm volatile("s_waitcnt " cntstr : "+v"(ru4[S][0]), "+v"(ru4[S][1]), "+v"(ru4[S][2]), "+v"(ru4[S][3]) :: "memory")
;     ...
;     {
;         unsigned er[PE_RD];
; #pragma unroll
;         for (int q = 0; q < PE_RD; ++q) { const v4u rec = *(const LAS v4u*)(ents + 4 * q); er[q] = __builtin_amdgcn_readfirstlane(rec.x); PE_ISSUE_U(q, rec); }
;         int jcur = (int)((er[0] >> 14) & 3u);
;         v4u hcur = *(const LAS v4u*)(hql + (jcur * 64 + lane) * 4);
;         v4u nrec = *(const LAS v4u*)(ents + 4 * PE_RD);
; #pragma unroll 1
;         for (int bi = 0; bi < nb; bi += PE_RD) {
; #pragma unroll
;             for (int q = 0; q < PE_RD; ++q) {
;                 PE_WAIT4U(q, PE_VMW);
;                 PE_UBATCH(q, er[q]);
;                 er[q] = __builtin_amdgcn_readfirstlane(nrec.x);
;                 PE_ISSUE_U(q, nrec);
;                 nrec = *(const LAS v4u*)(ents + 4 * (bi + q + PE_RD + 1));
;             }
;         }
.LBB0_2832:
	s_or_b64 exec, exec, s[0:1]
	v_cmp_gt_i32_e32 vcc, 6, v50
	s_and_saveexec_b64 s[0:1], vcc
	v_add_u32_e32 v0, s6, v50
	v_lshl_add_u32 v0, v0, 4, s90
	ds_write_b128 v0, v[122:125] offset:6720
	s_or_b64 exec, exec, s[0:1]
	s_waitcnt lgkmcnt(0)
	v_mov_b32_e32 v5, s90
	ds_read_b128 v[0:3], v5 offset:6720
	v_lshlrev_b32_e32 v118, 3, v50
	v_and_b32_e32 v43, 31, v50
	v_cmp_lt_u32_e64 s[100:101], 31, v50
	v_lshlrev_b32_e32 v43, 4, v43
	v_lshl_add_u32 v52, v43, 1, s90
	s_cmp_gt_i32 s6, 0
	s_cselect_b64 s[2:3], -1, 0
	s_cmp_lt_i32 s6, 1
	s_waitcnt lgkmcnt(0)
	v_readfirstlane_b32 s10, v0
	v_and_b32_e32 v48, 0x3fff, v0
	v_cndmask_b32_e64 v48, v48, v1, s[100:101]
	v_lshl_add_u32 v48, v48, 9, v43
	global_load_dwordx4 v[8:11], v48, s[70:71]
	v_cndmask_b32_e64 v48, v2, v3, s[100:101]
	v_lshl_add_u32 v48, v48, 9, v43
	global_load_dwordx4 v[12:15], v48, s[70:71]
	ds_read_b128 v[0:3], v5 offset:6736
	s_waitcnt lgkmcnt(0)
	v_readfirstlane_b32 s11, v0
	v_and_b32_e32 v48, 0x3fff, v0
	v_cndmask_b32_e64 v48, v48, v1, s[100:101]
	v_lshl_add_u32 v48, v48, 9, v43
	global_load_dwordx4 v[16:19], v48, s[70:71]
	v_cndmask_b32_e64 v48, v2, v3, s[100:101]
	v_lshl_add_u32 v48, v48, 9, v43
	global_load_dwordx4 v[20:23], v48, s[70:71]
	ds_read_b128 v[0:3], v5 offset:6752
	s_waitcnt lgkmcnt(0)
	v_readfirstlane_b32 s12, v0
	v_and_b32_e32 v48, 0x3fff, v0
	v_cndmask_b32_e64 v48, v48, v1, s[100:101]
	v_lshl_add_u32 v48, v48, 9, v43
	global_load_dwordx4 v[24:27], v48, s[70:71]
	v_cndmask_b32_e64 v48, v2, v3, s[100:101]
	v_lshl_add_u32 v48, v48, 9, v43
	global_load_dwordx4 v[28:31], v48, s[70:71]
	s_cbranch_scc1 .LBB0_2861
	s_bfe_u32 s9, s10, 0x2000e
	v_lshl_add_u32 v48, s9, 10, v52
	ds_read_b128 v[0:3], v48 offset:11072
	ds_read_b128 v[44:47], v48 offset:11088
	v_and_b32_e32 v4, 15, v50
	v_bfe_u32 v33, v50, 4, 1
	v_cmp_eq_u32_e32 vcc, 0, v4
	v_lshrrev_b32_e32 v4, 5, v50
	s_mov_b32 s7, 0
	v_lshl_add_u32 v33, v33, 1, v4
	v_readlane_b32 s8, v255, 2
	s_nop 1
.LBB0_2838:
	v_mov_b32_e32 v4, s8
	ds_read_b128 v[4:7], v4
	s_waitcnt vmcnt(4)
	s_bfe_u32 s0, s10, 0x30010
	s_cmp_lg_u32 s0, 0
	s_cbranch_scc0 .Lu16_skip0
	s_bfe_u32 s1, s10, 0x2000e
	s_cmp_eq_u32 s1, s9
	s_cbranch_scc1 .Lu16_same0
	v_lshl_add_u32 v48, s1, 10, v52
	ds_read_b128 v[0:3], v48 offset:11072
	ds_read_b128 v[44:47], v48 offset:11088
	s_mov_b32 s9, s1
.Lu16_same0:
	s_waitcnt lgkmcnt(0)
	v_dot8_i32_i4 v39, v8, v0, 0
	v_dot8_i32_i4 v40, v12, v0, 0
	v_dot8_i32_i4 v35, v8, v2, 0
	v_dot8_i32_i4 v36, v12, v2, 0
	v_dot8_i32_i4 v39, v9, v1, v39
	v_dot8_i32_i4 v40, v13, v1, v40
	v_dot8_i32_i4 v35, v9, v3, v35
	v_dot8_i32_i4 v36, v13, v3, v36
	v_dot8_i32_i4 v39, v10, v44, v39
	v_dot8_i32_i4 v40, v14, v44, v40
	v_dot8_i32_i4 v35, v10, v46, v35
	v_dot8_i32_i4 v36, v14, v46, v36
	v_dot8_i32_i4 v39, v11, v45, v39
	v_dot8_i32_i4 v40, v15, v45, v40
	v_dot8_i32_i4 v35, v11, v47, v35
	v_dot8_i32_i4 v36, v15, v47, v36
	s_nop 2
	v_lshl_add_u32 v39, v39, 4, v35
	v_lshl_add_u32 v40, v40, 4, v36
	s_mulk_i32 s1, 0x690
	s_nop 0
	v_permlane16_swap_b32_e32 v39, v40
	v_add_u32_e32 v39, v39, v40
	s_lshr_b32 s4, s10, 17
	s_add_i32 s1, s90, s1
	v_add_u32_dpp v39, v39, v39 quad_perm:[1,0,3,2] row_mask:0xf bank_mask:0xf bound_ctrl:1
	s_and_b32 s4, s4, 0x7ffc
	s_add_i32 s1, s1, s4
	v_add_u32_dpp v39, v39, v39 quad_perm:[2,3,0,1] row_mask:0xf bank_mask:0xf bound_ctrl:1
	v_lshl_add_u32 v34, v33, 2, s1
	s_nop 0
	v_add_u32_dpp v41, v39, v39 row_half_mirror row_mask:0xf bank_mask:0xf bound_ctrl:1
	s_nop 1
	v_mov_b32_dpp v42, v41 row_mirror row_mask:0xf bank_mask:0xf bound_ctrl:1
	v_add_u32_e32 v42, v41, v42
	s_and_saveexec_b64 s[0:1], vcc
	ds_write_b32 v34, v42
	s_or_b64 exec, exec, s[0:1]
.Lu16_skip0:
	s_waitcnt lgkmcnt(0)
	v_readfirstlane_b32 s10, v4
	v_and_b32_e32 v48, 0x3fff, v4
	v_cndmask_b32_e64 v48, v48, v5, s[100:101]
	v_lshl_add_u32 v48, v48, 9, v43
	global_load_dwordx4 v[8:11], v48, s[70:71]
	v_cndmask_b32_e64 v48, v6, v7, s[100:101]
	v_lshl_add_u32 v48, v48, 9, v43
	global_load_dwordx4 v[12:15], v48, s[70:71]
	v_mov_b32_e32 v4, s8
	ds_read_b128 v[4:7], v4 offset:16
	s_waitcnt vmcnt(4)
	s_bfe_u32 s0, s11, 0x30010
	s_cmp_lg_u32 s0, 0
	s_cbranch_scc0 .Lu16_skip1
	s_bfe_u32 s1, s11, 0x2000e
	s_cmp_eq_u32 s1, s9
	s_cbranch_scc1 .Lu16_same1
	v_lshl_add_u32 v48, s1, 10, v52
	ds_read_b128 v[0:3], v48 offset:11072
	ds_read_b128 v[44:47], v48 offset:11088
	s_mov_b32 s9, s1
; #define LAS __attribute__((address_space(3)))
; #define PE_VMW "vmcnt(" PE_STR(PE_VMY) ")"
; #define PE_ISSUE_U(S, rec_) PE_ISSUE4(S, rec_, UB8)
; #define PE_WAIT4U(S, cntstr) asm volatile("s_waitcnt " cntstr : "+v"(ru4[S][0]), "+v"(ru4[S][1]), "+v"(ru4[S][2]), "+v"(ru4[S][3]) :: "memory")
;     ...
;     {
;         unsigned er[PE_RD];
; #pragma unroll
;         for (int q = 0; q < PE_RD; ++q) { const v4u rec = *(const LAS v4u*)(ents + 4 * q); er[q] = __builtin_amdgcn_readfirstlane(rec.x); PE_ISSUE_U(q, rec); }
;         int jcur = (int)((er[0] >> 14) & 3u);
;         v4u hcur = *(const LAS v4u*)(hql + (jcur * 64 + lane) * 4);
;         v4u nrec = *(const LAS v4u*)(ents + 4 * PE_RD);
; #pragma unroll 1
;         for (int bi = 0; bi < nb; bi += PE_RD) {
; #pragma unroll
;             for (int q = 0; q < PE_RD; ++q) {
;                 PE_WAIT4U(q, PE_VMW);
;                 PE_UBATCH(q, er[q]);
;                 er[q] = __builtin_amdgcn_readfirstlane(nrec.x);
;                 PE_ISSUE_U(q, nrec);
;                 nrec = *(const LAS v4u*)(ents + 4 * (bi + q + PE_RD + 1));
;             }
.Lu16_same1:
	s_waitcnt lgkmcnt(0)
	v_dot8_i32_i4 v39, v16, v0, 0
	v_dot8_i32_i4 v40, v20, v0, 0
	v_dot8_i32_i4 v35, v16, v2, 0
	v_dot8_i32_i4 v36, v20, v2, 0
	v_dot8_i32_i4 v39, v17, v1, v39
	v_dot8_i32_i4 v40, v21, v1, v40
	v_dot8_i32_i4 v35, v17, v3, v35
	v_dot8_i32_i4 v36, v21, v3, v36
	v_dot8_i32_i4 v39, v18, v44, v39
	v_dot8_i32_i4 v40, v22, v44, v40
	v_dot8_i32_i4 v35, v18, v46, v35
	v_dot8_i32_i4 v36, v22, v46, v36
	v_dot8_i32_i4 v39, v19, v45, v39
	v_dot8_i32_i4 v40, v23, v45, v40
	v_dot8_i32_i4 v35, v19, v47, v35
	v_dot8_i32_i4 v36, v23, v47, v36
	s_nop 2
	v_lshl_add_u32 v39, v39, 4, v35
	v_lshl_add_u32 v40, v40, 4, v36
	s_mulk_i32 s1, 0x690
	s_nop 0
	v_permlane16_swap_b32_e32 v39, v40
	v_add_u32_e32 v39, v39, v40
	s_lshr_b32 s4, s11, 17
	s_add_i32 s1, s90, s1
	v_add_u32_dpp v39, v39, v39 quad_perm:[1,0,3,2] row_mask:0xf bank_mask:0xf bound_ctrl:1
	s_and_b32 s4, s4, 0x7ffc
	s_add_i32 s1, s1, s4
	v_add_u32_dpp v39, v39, v39 quad_perm:[2,3,0,1] row_mask:0xf bank_mask:0xf bound_ctrl:1
	v_lshl_add_u32 v34, v33, 2, s1
	s_nop 0
	v_add_u32_dpp v41, v39, v39 row_half_mirror row_mask:0xf bank_mask:0xf bound_ctrl:1
	s_nop 1
	v_mov_b32_dpp v42, v41 row_mirror row_mask:0xf bank_mask:0xf bound_ctrl:1
	v_add_u32_e32 v42, v41, v42
	s_and_saveexec_b64 s[0:1], vcc
	ds_write_b32 v34, v42
	s_or_b64 exec, exec, s[0:1]
.Lu16_skip1:
	s_waitcnt lgkmcnt(0)
	v_readfirstlane_b32 s11, v4
	v_and_b32_e32 v48, 0x3fff, v4
	v_cndmask_b32_e64 v48, v48, v5, s[100:101]
	v_lshl_add_u32 v48, v48, 9, v43
	global_load_dwordx4 v[16:19], v48, s[70:71]
	v_cndmask_b32_e64 v48, v6, v7, s[100:101]
	v_lshl_add_u32 v48, v48, 9, v43
	global_load_dwordx4 v[20:23], v48, s[70:71]
	v_mov_b32_e32 v4, s8
	ds_read_b128 v[4:7], v4 offset:32
	s_waitcnt vmcnt(4)
	s_bfe_u32 s0, s12, 0x30010
	s_cmp_lg_u32 s0, 0
	s_cbranch_scc0 .Lu16_skip2
	s_bfe_u32 s1, s12, 0x2000e
	s_cmp_eq_u32 s1, s9
	s_cbranch_scc1 .Lu16_same2
	v_lshl_add_u32 v48, s1, 10, v52
	ds_read_b128 v[0:3], v48 offset:11072
	ds_read_b128 v[44:47], v48 offset:11088
	s_mov_b32 s9, s1
.Lu16_same2:
	s_waitcnt lgkmcnt(0)
	v_dot8_i32_i4 v39, v24, v0, 0
	v_dot8_i32_i4 v40, v28, v0, 0
	v_dot8_i32_i4 v35, v24, v2, 0
	v_dot8_i32_i4 v36, v28, v2, 0
	v_dot8_i32_i4 v39, v25, v1, v39
	v_dot8_i32_i4 v40, v29, v1, v40
	v_dot8_i32_i4 v35, v25, v3, v35
	v_dot8_i32_i4 v36, v29, v3, v36
	v_dot8_i32_i4 v39, v26, v44, v39
	v_dot8_i32_i4 v40, v30, v44, v40
	v_dot8_i32_i4 v35, v26, v46, v35
	v_dot8_i32_i4 v36, v30, v46, v36
	v_dot8_i32_i4 v39, v27, v45, v39
	v_dot8_i32_i4 v40, v31, v45, v40
	v_dot8_i32_i4 v35, v27, v47, v35
	v_dot8_i32_i4 v36, v31, v47, v36
	s_nop 2
	v_lshl_add_u32 v39, v39, 4, v35
	v_lshl_add_u32 v40, v40, 4, v36
	s_mulk_i32 s1, 0x690
	s_nop 0
	v_permlane16_swap_b32_e32 v39, v40
	v_add_u32_e32 v39, v39, v40
	s_lshr_b32 s4, s12, 17
	s_add_i32 s1, s90, s1
	v_add_u32_dpp v39, v39, v39 quad_perm:[1,0,3,2] row_mask:0xf bank_mask:0xf bound_ctrl:1
	s_and_b32 s4, s4, 0x7ffc
	s_add_i32 s1, s1, s4
	v_add_u32_dpp v39, v39, v39 quad_perm:[2,3,0,1] row_mask:0xf bank_mask:0xf bound_ctrl:1
	v_lshl_add_u32 v34, v33, 2, s1
	s_nop 0
	v_add_u32_dpp v41, v39, v39 row_half_mirror row_mask:0xf bank_mask:0xf bound_ctrl:1
	s_nop 1
	v_mov_b32_dpp v42, v41 row_mirror row_mask:0xf bank_mask:0xf bound_ctrl:1
	v_add_u32_e32 v42, v41, v42
	s_and_saveexec_b64 s[0:1], vcc
	ds_write_b32 v34, v42
	s_or_b64 exec, exec, s[0:1]
.Lu16_skip2:
	s_waitcnt lgkmcnt(0)
	v_readfirstlane_b32 s12, v4
	v_and_b32_e32 v48, 0x3fff, v4
	v_cndmask_b32_e64 v48, v48, v5, s[100:101]
	v_lshl_add_u32 v48, v48, 9, v43
	global_load_dwordx4 v[24:27], v48, s[70:71]
	v_cndmask_b32_e64 v48, v6, v7, s[100:101]
	v_lshl_add_u32 v48, v48, 9, v43
	global_load_dwordx4 v[28:31], v48, s[70:71]
	s_add_i32 s7, s7, 3
	s_add_i32 s8, s8, 48
	s_cmp_ge_i32 s7, s6
	s_cbranch_scc0 .LBB0_2838

; __global__ void __launch_bounds__(NWAVES * 64, 2) hybrid_fwd(Params P) {
	.amdhsa_kernel _Z10hybrid_fwd6Params
		.amdhsa_group_segment_fixed_size 0
		.amdhsa_private_segment_fixed_size 0
		.amdhsa_kernarg_size 496
		.amdhsa_user_sgpr_count 2
		.amdhsa_user_sgpr_dispatch_ptr 0
		.amdhsa_user_sgpr_queue_ptr 0
		.amdhsa_user_sgpr_kernarg_segment_ptr 1
		.amdhsa_user_sgpr_dispatch_id 0
		.amdhsa_user_sgpr_kernarg_preload_length 0
		.amdhsa_user_sgpr_kernarg_preload_offset 0
		.amdhsa_user_sgpr_private_segment_size 0
		.amdhsa_uses_dynamic_stack 0
		.amdhsa_enable_private_segment 0
		.amdhsa_system_sgpr_workgroup_id_x 1
		.amdhsa_system_sgpr_workgroup_id_y 0
		.amdhsa_system_sgpr_workgroup_id_z 0
		.amdhsa_system_sgpr_workgroup_info 0
		.amdhsa_system_vgpr_workitem_id 0
		.amdhsa_next_free_vgpr 256
		.amdhsa_next_free_sgpr 102
		.amdhsa_accum_offset 256
		.amdhsa_reserve_vcc 1
		.amdhsa_float_round_mode_32 0
		.amdhsa_float_round_mode_16_64 0
		.amdhsa_float_denorm_mode_32 3
		.amdhsa_float_denorm_mode_16_64 3
		.amdhsa_dx10_clamp 1
		.amdhsa_ieee_mode 1
		.amdhsa_fp16_overflow 0
		.amdhsa_tg_split 0
		.amdhsa_exception_fp_ieee_invalid_op 0
		.amdhsa_exception_fp_denorm_src 0
		.amdhsa_exception_fp_ieee_div_zero 0
		.amdhsa_exception_fp_ieee_overflow 0
		.amdhsa_exception_fp_ieee_underflow 0
		.amdhsa_exception_fp_ieee_inexact 0
		.amdhsa_exception_int_div_zero 0
	.end_amdhsa_kernel

; __global__ void __launch_bounds__(NWAVES * 64, 2) hybrid_fwd(Params P) {
amdhsa.kernels:
  - .agpr_count:     0
    .args:
      - .offset:         0
        .size:           240
        .value_kind:     by_value
      - .offset:         240
        .size:           4
        .value_kind:     hidden_block_count_x
      - .offset:         244
        .size:           4
        .value_kind:     hidden_block_count_y
      - .offset:         248
        .size:           4
        .value_kind:     hidden_block_count_z
      - .offset:         252
        .size:           2
        .value_kind:     hidden_group_size_x
      - .offset:         254
        .size:           2
        .value_kind:     hidden_group_size_y
      - .offset:         256
        .size:           2
        .value_kind:     hidden_group_size_z
      - .offset:         258
        .size:           2
        .value_kind:     hidden_remainder_x
      - .offset:         260
        .size:           2
        .value_kind:     hidden_remainder_y
      - .offset:         262
        .size:           2
        .value_kind:     hidden_remainder_z
      - .offset:         280
        .size:           8
        .value_kind:     hidden_global_offset_x
      - .offset:         288
        .size:           8
        .value_kind:     hidden_global_offset_y
      - .offset:         296
        .size:           8
        .value_kind:     hidden_global_offset_z
      - .offset:         304
        .size:           2
        .value_kind:     hidden_grid_dims
      - .offset:         360
        .size:           4
        .value_kind:     hidden_dynamic_lds_size
    .group_segment_fixed_size: 0
    .kernarg_segment_align: 8
    .kernarg_segment_size: 496
    .language:       OpenCL C
    .language_version:
      - 2
      - 0
    .max_flat_workgroup_size: 512
    .name:           _Z10hybrid_fwd6Params
    .private_segment_fixed_size: 0
    .sgpr_count:     108
    .sgpr_spill_count: 101
    .symbol:         _Z10hybrid_fwd6Params.kd
    .uniform_work_group_size: 1
    .uses_dynamic_stack: false
    .vgpr_count:     256
    .vgpr_spill_count: 0
    .wavefront_size: 64
